# warm64
# baseline (speedup 1.0000x reference)
_Z11prep_kernelPKfS0_PKiS2_S0_S0_S0_S0_S0_S0_Pc:
	s_load_dwordx4 s[28:31], s[0:1], 0x40
	s_load_dwordx8 s[12:19], s[0:1], 0x0
	s_load_dwordx8 s[20:27], s[0:1], 0x20
	s_load_dwordx2 s[32:33], s[0:1], 0x50
	s_load_dword s40, s[0:1], 0x80
	s_getpc_b64 s[36:37]
	s_add_u32 s36, s36, _Z11attn_kernelILi4EEvPKfS1_S1_S1_S1_S1_PKcPf@rel32@lo+4
	s_addc_u32 s37, s37, _Z11attn_kernelILi4EEvPKfS1_S1_S1_S1_S1_PKcPf@rel32@hi+12
	v_and_b32_e32 v192, 63, v0
	v_lshlrev_b32_e32 v192, 6, v192
	v_min_u32_e32 v193, 0x180, v192
	v_add_u32_e32 v193, 0x1000, v193
	global_load_dword v192, v192, s[36:37]
	global_load_dword v193, v193, s[36:37]
	s_lshr_b32 s4, s2, 2
	v_lshrrev_b32_e32 v2, 6, v0
	s_and_b32 s4, s4, 0x1ffffffe
	v_and_b32_e32 v1, 15, v0
	s_and_b32 s3, s2, 7
	v_or_b32_e32 v2, s4, v2
	v_lshl_or_b32 v88, v2, 3, s3
	v_cmp_gt_u32_e64 s[10:11], 14, v1
	v_mul_lo_u32 v7, v88, 14
	v_and_b32_e32 v105, 63, v0
	v_cndmask_b32_e64 v6, 13, v1, s[10:11]
	v_add_u32_e32 v2, v7, v6
	v_mul_u32_u24_e32 v4, 12, v2
	v_lshlrev_b32_e32 v5, 2, v6
	v_cmp_gt_u32_e64 s[8:9], 48, v105
	v_cmp_gt_u32_e64 s[6:7], 14, v105
	v_lshlrev_b32_e32 v118, 1, v0
	v_lshrrev_b32_e32 v104, 4, v0
	v_cndmask_b32_e64 v8, 0, v105, s[8:9]
	v_cndmask_b32_e64 v9, 0, v105, s[6:7]
	v_mad_u32_u24 v8, v88, 48, v8
	v_add_lshl_u32 v9, v7, v9, 2
	v_lshlrev_b32_e32 v8, 2, v8
	s_lshl_b32 s2, s2, 3
	s_and_b32 s2, s2, 0x78
	v_and_b32_e32 v106, 30, v118
	v_or_b32_e32 v107, s2, v104
	v_cmp_gt_u32_e64 s[2:3], 23, v106
	v_or_b32_e32 v10, 1, v106
	v_cmp_gt_u32_e64 s[4:5], 23, v10
	v_lshlrev_b32_e32 v11, 7, v106
	v_lshlrev_b32_e32 v10, 7, v10
	v_cndmask_b32_e64 v11, 0, v11, s[2:3]
	v_cndmask_b32_e64 v10, 0, v10, s[4:5]
	v_or_b32_e32 v11, v11, v107
	v_or_b32_e32 v10, v10, v107
	v_lshlrev_b32_e32 v11, 2, v11
	v_lshlrev_b32_e32 v10, 2, v10
	v_lshlrev_b32_e32 v12, 2, v107
	v_lshlrev_b32_e32 v119, 5, v0
	v_lshlrev_b32_e32 v13, 2, v0
	v_and_b32_e32 v109, 12, v13
	v_and_b32_e32 v91, 0xf80, v119
	v_lshl_or_b32 v91, v109, 2, v91
	v_or_b32_e32 v92, 0x1000, v91
	v_lshlrev_b32_e32 v90, 9, v2
	v_and_b32_e32 v16, 48, v0
	v_or_b32_e32 v90, v90, v16
	v_or_b32_e32 v112, 0x80, v0
	v_or_b32_e32 v111, 0x180, v0
	v_or_b32_e32 v108, 0x280, v0
	v_mov_b32_e32 v87, 0
	v_bfe_u32 v110, v0, 4, 2
	s_movk_i32 s34, 0x60
	v_lshrrev_b32_e32 v136, 1, v0
	v_lshrrev_b32_e32 v18, 3, v0
	v_and_b32_e32 v18, 4, v18
	v_and_b32_e32 v19, 24, v0
	v_and_b32_e32 v20, 2, v136
	v_or3_b32 v18, v18, v19, v20
	v_and_or_b32 v136, v136, s34, v18
	v_mul_u32_u24_e32 v18, 0x110, v109
	v_lshl_add_u32 v136, v136, 1, v18
	v_add_u32_e32 v137, 0x1100, v136
	v_add_u32_e32 v138, 0x2200, v136
	v_lshlrev_b32_e32 v18, 9, v88
	v_and_b32_e32 v19, 0x100, v119
	v_lshlrev_b32_e32 v20, 4, v0
	v_and_b32_e32 v20, 48, v20
	v_or3_b32 v139, v18, v19, v20
	v_and_b32_e32 v19, 8, v118
	v_and_b32_e32 v20, 64, v118
	v_or3_b32 v139, v139, v19, v20
	v_lshlrev_b32_e32 v19, 2, v110
	v_and_b32_e32 v20, 4, v19
	v_or_b32_e32 v139, v139, v20
	v_lshl_or_b32 v140, v1, 5, v18
	v_or_b32_e32 v140, v140, v19
	v_add_u32_e32 v140, 0x80000, v140
	v_lshl_or_b32 v141, v88, 4, v1
	v_lshlrev_b32_e32 v141, 3, v141
	v_add_u32_e32 v141, 0x140000, v141
	v_lshlrev_b32_e32 v20, 8, v88
	v_mul_u32_u24_e32 v21, 43, v105
	v_lshrrev_b32_e32 v21, 9, v21
	v_mul_u32_u24_e32 v21, 12, v21
	v_sub_u32_e32 v22, v105, v21
	v_and_b32_e32 v142, 3, v22
	v_lshrrev_b32_e32 v22, 2, v22
	v_mad_u32_u24 v142, v142, 3, v22
	v_add_u32_e32 v142, v142, v21
	v_lshl_add_u32 v142, v142, 2, v20
	v_add_u32_e32 v142, 0x164000, v142
	v_lshl_add_u32 v143, v105, 2, v20
	v_add_u32_e32 v143, 0x164000, v143
	v_lshlrev_b32_e32 v123, 6, v107
	v_lshl_add_u32 v123, v106, 1, v123
	v_add_u32_e32 v123, 0x160000, v123
	v_lshl_add_u32 v122, v1, 4, v20
	v_or_b32_e32 v122, v122, v19
	v_add_u32_e32 v122, 0x100000, v122
	s_waitcnt lgkmcnt(0)
	global_load_dwordx3 v[82:84], v4, s[12:13]
	global_load_dword v85, v5, s[26:27]
	global_load_dword v114, v8, s[18:19]
	global_load_dword v115, v9, s[16:17]
	global_load_dword v116, v11, s[28:29]
	global_load_dword v113, v10, s[28:29]
	global_load_dword v117, v12, s[30:31]
	global_load_dwordx4 v[66:69], v91, s[20:21]
	global_load_dwordx4 v[70:73], v91, s[20:21] offset:64
	global_load_dwordx4 v[74:77], v92, s[20:21]
	global_load_dwordx4 v[78:81], v92, s[20:21] offset:64
	global_load_dwordx4 v[58:61], v91, s[22:23]
	global_load_dwordx4 v[62:65], v91, s[22:23] offset:64
	global_load_dwordx4 v[50:53], v92, s[22:23]
	global_load_dwordx4 v[54:57], v92, s[22:23] offset:64
	global_load_dwordx4 v[42:45], v91, s[24:25]
	global_load_dwordx4 v[46:49], v91, s[24:25] offset:64
	global_load_dwordx4 v[34:37], v92, s[24:25]
	global_load_dwordx4 v[38:41], v92, s[24:25] offset:64
	global_load_dwordx4 v[26:29], v90, s[14:15] nt
	global_load_dwordx4 v[30:33], v90, s[14:15] offset:64 nt
	global_load_dwordx4 v[18:21], v90, s[14:15] offset:128 nt
	global_load_dwordx4 v[22:25], v90, s[14:15] offset:192 nt
	global_load_dwordx4 v[10:13], v90, s[14:15] offset:256 nt
	global_load_dwordx4 v[14:17], v90, s[14:15] offset:320 nt
	global_load_dwordx4 v[2:5], v90, s[14:15] offset:384 nt
	global_load_dwordx4 v[6:9], v90, s[14:15] offset:448 nt
	s_waitcnt vmcnt(26)
	v_mov_b32_e32 v90, v83
	v_mov_b32_e32 v91, v84
	v_lshlrev_b32_e32 v86, 2, v110
	s_waitcnt vmcnt(25)
	v_mul_f32_e32 v84, 0x3fb8aa3b, v85
	s_mov_b32 s14, 0x41700000
	v_exp_f32_e32 v84, v84
	v_cndmask_b32_e64 v94, 0, 1.0, s[10:11]
	v_add_f32_e32 v84, 1.0, v84
	v_cmp_lt_f32_e32 vcc, s14, v85
	v_log_f32_e32 v84, v84
	v_cmp_lt_u32_e64 s[12:13], 15, v105
	v_mul_f32_e32 v84, 0x3f317218, v84
	v_cndmask_b32_e32 v84, v84, v85, vcc
	v_mul_f32_e32 v84, 0xbe715bef, v84
	v_mul_f32_e32 v84, 0x3f3504f3, v84
	v_mul_f32_e32 v84, 0x41800000, v84
	v_cndmask_b32_e64 v99, 0, v84, s[10:11]
	v_mul_f32_e32 v101, -2.0, v99
	v_mul_f32_e32 v100, v82, v82
	v_cmp_gt_u32_e32 vcc, 16, v105
	v_fmac_f32_e32 v100, v90, v90
	v_cmp_eq_u32_e64 s[12:13], 0, v110
	v_fmac_f32_e32 v100, v91, v91
	v_cmp_eq_u32_e64 s[14:15], 1, v110
	v_mul_f32_e32 v83, v101, v82
	v_cmp_eq_u32_e64 s[16:17], 2, v110
	v_mul_f32_e32 v84, v101, v90
	v_mul_f32_e32 v85, v101, v91
	v_mul_f32_e32 v89, v99, v100
	v_mul_f32_e32 v92, v82, v94
	v_mul_f32_e32 v93, v90, v94
	v_mul_f32_e32 v95, v91, v94
	v_mul_f32_e32 v96, v100, v94
	v_cvt_pk_fp8_f32 v88, v83, v83
	v_cvt_pk_fp8_f32 v104, v84, v84
	v_cvt_f32_fp8_e32 v97, v88
	v_cvt_f32_fp8_e32 v98, v104
	v_sub_f32_e32 v97, v83, v97
	v_sub_f32_e32 v98, v84, v98
	v_cvt_pk_fp8_f32 v88, v85, v85
	v_cvt_pk_fp8_f32 v104, v99, v99
	v_cvt_f32_fp8_e32 v101, v88
	v_cvt_f32_fp8_e32 v102, v104
	v_sub_f32_e32 v101, v85, v101
	v_sub_f32_e32 v102, v99, v102
	v_cvt_pk_fp8_f32 v88, v89, v89
	v_cvt_pk_fp8_f32 v104, v92, v92
	v_cvt_f32_fp8_e32 v103, v88
	v_cvt_f32_fp8_e32 v120, v104
	v_sub_f32_e32 v103, v89, v103
	v_sub_f32_e32 v120, v92, v120
	v_cvt_pk_fp8_f32 v88, v93, v93
	v_cvt_pk_fp8_f32 v104, v95, v95
	v_cvt_f32_fp8_e32 v121, v88
	v_cvt_f32_fp8_e32 v86, v104
	v_sub_f32_e32 v121, v93, v121
	v_sub_f32_e32 v86, v95, v86
	v_cvt_pk_fp8_f32 v88, v96, v96
	s_nop 0
	v_cvt_f32_fp8_e32 v87, v88
	s_nop 0
	v_sub_f32_e32 v87, v96, v87
	v_cndmask_b32_e64 v124, v89, v85, s[16:17]
	v_cndmask_b32_e64 v124, v124, v98, s[14:15]
	v_cndmask_b32_e64 v124, v124, v83, s[12:13]
	v_cndmask_b32_e64 v125, v103, v99, s[16:17]
	v_cndmask_b32_e64 v125, v125, v84, s[14:15]
	v_cndmask_b32_e64 v125, v125, v97, s[12:13]
	v_cndmask_b32_e64 v126, 0, v102, s[16:17]
	v_cndmask_b32_e64 v126, v126, v85, s[14:15]
	v_cndmask_b32_e64 v126, v126, v83, s[12:13]
	v_cndmask_b32_e64 v127, 0, v99, s[16:17]
	v_cndmask_b32_e64 v127, v127, v101, s[14:15]
	v_cndmask_b32_e64 v127, v127, v84, s[12:13]
	v_cndmask_b32_e64 v128, v94, v86, s[16:17]
	v_cndmask_b32_e64 v128, v128, v93, s[14:15]
	v_cndmask_b32_e64 v128, v128, v92, s[12:13]
	v_cndmask_b32_e64 v129, v94, v96, s[16:17]
	v_cndmask_b32_e64 v129, v129, v121, s[14:15]
	v_cndmask_b32_e64 v129, v129, v92, s[12:13]
	v_cndmask_b32_e64 v130, 0, v96, s[16:17]
	v_cndmask_b32_e64 v130, v130, v95, s[14:15]
	v_cndmask_b32_e64 v130, v130, v120, s[12:13]
	v_cndmask_b32_e64 v131, 0, v87, s[16:17]
	v_cndmask_b32_e64 v131, v131, v95, s[14:15]
	v_cndmask_b32_e64 v131, v131, v93, s[12:13]
	v_cvt_pk_fp8_f32 v119, v124, v125
	v_cvt_pk_fp8_f32 v103, v128, v129
	v_cvt_pk_fp8_f32 v119, v126, v127 op_sel:[0,0,1]
	v_cvt_pk_fp8_f32 v103, v130, v131 op_sel:[0,0,1]
	s_nop 0
	global_store_dword v139, v119, s[32:33] offset:128
	global_store_dword v140, v103, s[32:33] offset:16
	s_and_saveexec_b64 s[0:1], vcc
	s_cbranch_execz .LBB0_14
	v_cvt_f16_f32_e32 v83, v82
	v_cvt_pk_f16_f32 v90, v90, v91
	s_nop 0
	v_alignbit_b32 v91, 0, v90, 16
	v_pack_b32_f16 v90, v83, v90
	global_store_dwordx2 v141, v[90:91], s[32:33]
